# attention: scale folded into one fma per score, next K/V requests issued between the QK MFMAs
# baseline (speedup 1.0000x reference)
.Lcv_a_nop:
	s_waitcnt lgkmcnt(0)
	v_add_u32_e32 v2, 31, v172
	v_and_b32_e32 v173, 15, v151
	v_ashrrev_i32_e32 v174, 4, v151
	v_ashrrev_i32_e32 v176, 5, v2
	v_mov_b32_e32 v29, 0
	v_lshlrev_b32_e32 v148, 7, v173
	v_mov_b32_e32 v149, v147
	v_cmp_lt_i32_e32 vcc, 0, v176
	v_lshlrev_b32_e32 v150, 2, v174
	v_mov_b32_e32 v28, v29
	v_mov_b32_e32 v27, v29
	v_mov_b32_e32 v26, v29
	v_mov_b32_e32 v33, v29
	v_mov_b32_e32 v32, v29
	v_mov_b32_e32 v31, v29
	v_mov_b32_e32 v30, v29
	v_mov_b32_e32 v25, v29
	v_mov_b32_e32 v24, v29
	v_mov_b32_e32 v23, v29
	v_mov_b32_e32 v22, v29
	v_mov_b32_e32 v21, v29
	v_mov_b32_e32 v20, v29
	v_mov_b32_e32 v19, v29
	v_mov_b32_e32 v18, v29
	v_mov_b32_e32 v17, v29
	v_mov_b32_e32 v16, v29
	v_mov_b32_e32 v15, v29
	v_mov_b32_e32 v14, v29
	v_mov_b32_e32 v13, v29
	v_mov_b32_e32 v12, v29
	v_mov_b32_e32 v11, v29
	v_mov_b32_e32 v10, v29
	v_mov_b32_e32 v9, v29
	v_mov_b32_e32 v8, v29
	v_mov_b32_e32 v7, v29
	v_mov_b32_e32 v6, v29
	v_mov_b32_e32 v5, v29
	v_mov_b32_e32 v4, v29
	v_mov_b32_e32 v3, v29
	v_mov_b32_e32 v2, v29
	v_mov_b32_e32 v179, v29
	s_and_saveexec_b64 s[0:1], vcc
	s_cbranch_execz .LBB0_1127
	v_readfirstlane_b32 s10, v176
	v_readfirstlane_b32 s36, v172
	v_readlane_b32 s37, v242, 49
	s_mul_i32 s5, s78, 0x3400000
	s_mul_hi_i32 s4, s78, 0x3400000
	s_add_u32 s2, s82, s5
	s_addc_u32 s3, s83, s4
	s_add_u32 s4, s2, 0x2800
	s_addc_u32 s5, s3, 0
	s_add_u32 s6, s2, 0x2900
	s_addc_u32 s7, s3, 0
	s_mul_i32 s20, s97, 0x3400
	s_mul_hi_u32 s21, s96, 0x3400
	s_add_i32 s21, s21, s20
	s_mul_i32 s20, s96, 0x3400
	s_add_u32 s20, s82, s20
	s_addc_u32 s21, s83, s21
	s_add_u32 s20, s20, 0x1800
	s_addc_u32 s21, s21, 0
	s_add_u32 s26, s89, 0x400
	s_lshl_b32 s27, s37, 13
	s_add_u32 s27, s27, 0x14000
	v_lshlrev_b32_e32 v96, 2, v150
	v_lshl_add_u32 v153, v148, 1, v96
	global_load_dwordx4 v[42:45], v153, s[20:21]
	global_load_dwordx4 v[34:37], v153, s[20:21] offset:64
	global_load_dwordx4 v[38:41], v153, s[20:21] offset:128
	global_load_dwordx4 v[46:49], v153, s[20:21] offset:192
	v_add_u32_e32 v239, s89, v150
	ds_read2_b32 v[98:99], v239 offset0:0 offset1:4
	ds_read2_b32 v[100:101], v239 offset0:8 offset1:12
	ds_read2_b32 v[102:103], v239 offset0:16 offset1:20
	ds_read2_b32 v[104:105], v239 offset0:24 offset1:28
	ds_read2_b32 v[106:107], v239 offset0:32 offset1:36
	ds_read2_b32 v[108:109], v239 offset0:40 offset1:44
	ds_read2_b32 v[110:111], v239 offset0:48 offset1:52
	ds_read2_b32 v[112:113], v239 offset0:56 offset1:60
	v_mov_b32_e32 v96, v174
	v_xor_b32_e32 v96, v96, v173
	v_lshlrev_b32_e32 v220, 4, v96
	v_add_u32_e32 v96, 4, v174
	v_xor_b32_e32 v96, v96, v173
	v_lshlrev_b32_e32 v221, 4, v96
	v_add_u32_e32 v96, 8, v174
	v_xor_b32_e32 v96, v96, v173
	v_lshlrev_b32_e32 v222, 4, v96
	v_add_u32_e32 v96, 12, v174
	v_xor_b32_e32 v96, v96, v173
	v_lshlrev_b32_e32 v223, 4, v96
	v_lshlrev_b32_e32 v224, 4, v173
	v_lshlrev_b32_e32 v96, 1, v174
	v_xor_b32_e32 v96, v96, v173
	v_lshlrev_b32_e32 v96, 4, v96
	v_lshl_add_u32 v97, v174, 8, s27
	v_add_u32_e32 v225, v97, v96
	v_xor_b32_e32 v96, 0x80, v96
	v_add_u32_e32 v226, v97, v96
	v_lshl_add_u32 v97, v173, 8, s26
	v_mov_b32_e32 v96, v174
	v_xor_b32_e32 v96, v96, v173
	v_lshl_add_u32 v227, v96, 4, v97
	v_add_u32_e32 v96, 4, v174
	v_xor_b32_e32 v96, v96, v173
	v_lshl_add_u32 v228, v96, 4, v97
	v_add_u32_e32 v96, 8, v174
	v_xor_b32_e32 v96, v96, v173
	v_lshl_add_u32 v229, v96, 4, v97
	v_add_u32_e32 v96, 12, v174
	v_xor_b32_e32 v96, v96, v173
	v_lshl_add_u32 v230, v96, 4, v97
	v_lshrrev_b32_e32 v241, 2, v173
	v_add_u32_e32 v241, v241, v150
	v_and_b32_e32 v177, 7, v241
	v_and_b32_e32 v96, 3, v173
	v_lshlrev_b32_e32 v96, 3, v96
	v_lshl_add_u32 v241, v241, 8, v96
	v_add_u32_e32 v241, s27, v241
	v_xor_b32_e32 v96, 0, v177
	v_lshl_add_u32 v231, v96, 5, v241
	v_xor_b32_e32 v96, 1, v177
	v_lshl_add_u32 v232, v96, 5, v241
	v_xor_b32_e32 v96, 2, v177
	v_lshl_add_u32 v233, v96, 5, v241
	v_xor_b32_e32 v96, 3, v177
	v_lshl_add_u32 v234, v96, 5, v241
	v_xor_b32_e32 v96, 4, v177
	v_lshl_add_u32 v235, v96, 5, v241
	v_xor_b32_e32 v96, 5, v177
	v_lshl_add_u32 v236, v96, 5, v241
	v_xor_b32_e32 v96, 6, v177
	v_lshl_add_u32 v237, v96, 5, v241
	v_xor_b32_e32 v96, 7, v177
	v_lshl_add_u32 v238, v96, 5, v241
	v_mov_b32_e32 v2, 0
	v_mov_b32_e32 v3, 0
	v_mov_b32_e32 v4, 0
	v_mov_b32_e32 v5, 0
	v_mov_b32_e32 v6, 0
	v_mov_b32_e32 v7, 0
	v_mov_b32_e32 v8, 0
	v_mov_b32_e32 v9, 0
	v_mov_b32_e32 v10, 0
	v_mov_b32_e32 v11, 0
	v_mov_b32_e32 v12, 0
	v_mov_b32_e32 v13, 0
	v_mov_b32_e32 v14, 0
	v_mov_b32_e32 v15, 0
	v_mov_b32_e32 v16, 0
	v_mov_b32_e32 v17, 0
	v_mov_b32_e32 v18, 0
	v_mov_b32_e32 v19, 0
	v_mov_b32_e32 v20, 0
	v_mov_b32_e32 v21, 0
	v_mov_b32_e32 v22, 0
	v_mov_b32_e32 v23, 0
	v_mov_b32_e32 v24, 0
	v_mov_b32_e32 v25, 0
	v_mov_b32_e32 v26, 0
	v_mov_b32_e32 v27, 0
	v_mov_b32_e32 v28, 0
	v_mov_b32_e32 v29, 0
	v_mov_b32_e32 v30, 0
	v_mov_b32_e32 v31, 0
	v_mov_b32_e32 v32, 0
	v_mov_b32_e32 v33, 0
	v_mov_b32_e32 v179, 0
	v_mov_b32_e32 v181, 0xf149f2ca
	v_mov_b32_e32 v95, 0
	s_mov_b32 s11, 0
	s_mov_b32 s22, 0
	s_mov_b32 s25, 0x3e0293ee
	s_waitcnt lgkmcnt(0)
	s_mov_b32 m0, s26
	v_mad_u32_u24 v240, v98, s35, v220
	global_load_lds_dwordx4 v240, s[4:5]
	s_add_u32 m0, s26, 1024
	v_mad_u32_u24 v240, v99, s35, v221
	global_load_lds_dwordx4 v240, s[4:5]
	s_add_u32 m0, s26, 2048
	v_mad_u32_u24 v240, v100, s35, v222
	global_load_lds_dwordx4 v240, s[4:5]
	s_add_u32 m0, s26, 3072
	v_mad_u32_u24 v240, v101, s35, v223
	global_load_lds_dwordx4 v240, s[4:5]
	s_add_u32 m0, s26, 4096
	v_mad_u32_u24 v240, v102, s35, v220
	global_load_lds_dwordx4 v240, s[4:5]
	s_add_u32 m0, s26, 5120
	v_mad_u32_u24 v240, v103, s35, v221
	global_load_lds_dwordx4 v240, s[4:5]
	s_add_u32 m0, s26, 6144
	v_mad_u32_u24 v240, v104, s35, v222
	global_load_lds_dwordx4 v240, s[4:5]
	s_add_u32 m0, s26, 7168
	v_mad_u32_u24 v240, v105, s35, v223
	global_load_lds_dwordx4 v240, s[4:5]
	v_mad_u32_u24 v240, v98, s35, v224
	global_load_dwordx4 v[114:117], v240, s[6:7]
	v_mad_u32_u24 v240, v99, s35, v224
	global_load_dwordx4 v[118:121], v240, s[6:7]
	v_mad_u32_u24 v240, v100, s35, v224
	global_load_dwordx4 v[122:125], v240, s[6:7]
	v_mad_u32_u24 v240, v101, s35, v224
	global_load_dwordx4 v[126:129], v240, s[6:7]
	v_mad_u32_u24 v240, v102, s35, v224
	global_load_dwordx4 v[130:133], v240, s[6:7]
	v_mad_u32_u24 v240, v103, s35, v224
	global_load_dwordx4 v[134:137], v240, s[6:7]
	v_mad_u32_u24 v240, v104, s35, v224
	global_load_dwordx4 v[138:141], v240, s[6:7]
	v_mad_u32_u24 v240, v105, s35, v224
	global_load_dwordx4 v[142:145], v240, s[6:7]
	s_cmp_ge_u32 s10, 2
	s_cbranch_scc0 .Lat_A
	v_mad_u32_u24 v240, v106, s35, v224
	global_load_dwordx4 v[188:191], v240, s[6:7]
	v_mad_u32_u24 v240, v107, s35, v224
	global_load_dwordx4 v[192:195], v240, s[6:7]
	v_mad_u32_u24 v240, v108, s35, v224
	global_load_dwordx4 v[196:199], v240, s[6:7]
	v_mad_u32_u24 v240, v109, s35, v224
	global_load_dwordx4 v[200:203], v240, s[6:7]
	v_mad_u32_u24 v240, v110, s35, v224
	global_load_dwordx4 v[204:207], v240, s[6:7]
	v_mad_u32_u24 v240, v111, s35, v224
	global_load_dwordx4 v[208:211], v240, s[6:7]
	v_mad_u32_u24 v240, v112, s35, v224
	global_load_dwordx4 v[212:215], v240, s[6:7]
	v_mad_u32_u24 v240, v113, s35, v224
	global_load_dwordx4 v[216:219], v240, s[6:7]

.Lat_A_nosel:
	s_waitcnt lgkmcnt(0)
	s_cmp_ge_u32 s23, 3
	s_cbranch_scc0 .Lat_A_tail
	v_mfma_f32_16x16x32_bf16 v[82:85], v[50:53], v[42:45], 0
	s_mov_b32 m0, s26
	v_mad_u32_u24 v240, v106, s35, v220
	global_load_lds_dwordx4 v240, s[4:5]
	s_add_u32 m0, s26, 1024
	v_mad_u32_u24 v240, v107, s35, v221
	global_load_lds_dwordx4 v240, s[4:5]
	v_mfma_f32_16x16x32_bf16 v[86:89], v[66:69], v[42:45], 0
	s_add_u32 m0, s26, 2048
	v_mad_u32_u24 v240, v108, s35, v222
	global_load_lds_dwordx4 v240, s[4:5]
	s_add_u32 m0, s26, 3072
	v_mad_u32_u24 v240, v109, s35, v223
	global_load_lds_dwordx4 v240, s[4:5]
	v_mfma_f32_16x16x32_bf16 v[82:85], v[54:57], v[34:37], v[82:85]
	s_add_u32 m0, s26, 4096
	v_mad_u32_u24 v240, v110, s35, v220
	global_load_lds_dwordx4 v240, s[4:5]
	s_add_u32 m0, s26, 5120
	v_mad_u32_u24 v240, v111, s35, v221
	global_load_lds_dwordx4 v240, s[4:5]
	v_mfma_f32_16x16x32_bf16 v[86:89], v[70:73], v[34:37], v[86:89]
	s_add_u32 m0, s26, 6144
	v_mad_u32_u24 v240, v112, s35, v222
	global_load_lds_dwordx4 v240, s[4:5]
	s_add_u32 m0, s26, 7168
	v_mad_u32_u24 v240, v113, s35, v223
	global_load_lds_dwordx4 v240, s[4:5]
	v_mfma_f32_16x16x32_bf16 v[82:85], v[58:61], v[38:41], v[82:85]
	v_mad_u32_u24 v240, v98, s35, v224
	global_load_dwordx4 v[114:117], v240, s[6:7]
	v_mad_u32_u24 v240, v99, s35, v224
	global_load_dwordx4 v[118:121], v240, s[6:7]
	v_mfma_f32_16x16x32_bf16 v[86:89], v[74:77], v[38:41], v[86:89]
	v_mad_u32_u24 v240, v100, s35, v224
	global_load_dwordx4 v[122:125], v240, s[6:7]
	v_mad_u32_u24 v240, v101, s35, v224
	global_load_dwordx4 v[126:129], v240, s[6:7]
	v_mfma_f32_16x16x32_bf16 v[82:85], v[62:65], v[46:49], v[82:85]
	v_mad_u32_u24 v240, v102, s35, v224
	global_load_dwordx4 v[130:133], v240, s[6:7]
	v_mad_u32_u24 v240, v103, s35, v224
	global_load_dwordx4 v[134:137], v240, s[6:7]
	v_mfma_f32_16x16x32_bf16 v[86:89], v[78:81], v[46:49], v[86:89]
	v_mad_u32_u24 v240, v104, s35, v224
	global_load_dwordx4 v[138:141], v240, s[6:7]
	v_mad_u32_u24 v240, v105, s35, v224
	global_load_dwordx4 v[142:145], v240, s[6:7]
	s_branch .Lat_A_sm
.Lat_A_tail:
	s_cmp_ge_u32 s23, 2
	s_cbranch_scc0 .Lat_A_nok
	s_mov_b32 m0, s26
	v_mad_u32_u24 v240, v106, s35, v220
	global_load_lds_dwordx4 v240, s[4:5]
	s_add_u32 m0, s26, 1024
	v_mad_u32_u24 v240, v107, s35, v221
	global_load_lds_dwordx4 v240, s[4:5]
	s_add_u32 m0, s26, 2048
	v_mad_u32_u24 v240, v108, s35, v222
	global_load_lds_dwordx4 v240, s[4:5]
	s_add_u32 m0, s26, 3072
	v_mad_u32_u24 v240, v109, s35, v223
	global_load_lds_dwordx4 v240, s[4:5]
	s_add_u32 m0, s26, 4096
	v_mad_u32_u24 v240, v110, s35, v220
	global_load_lds_dwordx4 v240, s[4:5]
	s_add_u32 m0, s26, 5120
	v_mad_u32_u24 v240, v111, s35, v221
	global_load_lds_dwordx4 v240, s[4:5]
	s_add_u32 m0, s26, 6144
	v_mad_u32_u24 v240, v112, s35, v222
	global_load_lds_dwordx4 v240, s[4:5]
	s_add_u32 m0, s26, 7168
	v_mad_u32_u24 v240, v113, s35, v223
	global_load_lds_dwordx4 v240, s[4:5]

.Lat_A_sm:
	v_add_u32_e32 v90, s22, v150
	v_add_u32_e32 v91, 16, v90
	s_add_u32 s24, s22, 32
	s_nop 6
	s_cmp_le_u32 s24, s36
	s_cbranch_scc1 .Lat_A_full
	v_add_u32_e32 v92, 0, v90
	v_cmp_lt_i32_e32 vcc, v92, v172
	v_add_u32_e32 v93, 0, v91
	s_nop 1
	v_cndmask_b32_e32 v82, v170, v82, vcc
	v_cmp_lt_i32_e32 vcc, v93, v172
	s_nop 1
	s_nop 0
	v_cndmask_b32_e32 v86, v170, v86, vcc
	v_add_u32_e32 v92, 1, v90
	v_cmp_lt_i32_e32 vcc, v92, v172
	v_add_u32_e32 v93, 1, v91
	s_nop 1
	v_cndmask_b32_e32 v83, v170, v83, vcc
	v_cmp_lt_i32_e32 vcc, v93, v172
	s_nop 1
	s_nop 0
	v_cndmask_b32_e32 v87, v170, v87, vcc
	v_add_u32_e32 v92, 2, v90
	v_cmp_lt_i32_e32 vcc, v92, v172
	v_add_u32_e32 v93, 2, v91
	s_nop 1
	v_cndmask_b32_e32 v84, v170, v84, vcc
	v_cmp_lt_i32_e32 vcc, v93, v172
	s_nop 1
	s_nop 0
	v_cndmask_b32_e32 v88, v170, v88, vcc
	v_add_u32_e32 v92, 3, v90
	v_cmp_lt_i32_e32 vcc, v92, v172
	v_add_u32_e32 v93, 3, v91
	s_nop 1
	v_cndmask_b32_e32 v85, v170, v85, vcc
	v_cmp_lt_i32_e32 vcc, v93, v172
	s_nop 1
	s_nop 0
	v_cndmask_b32_e32 v89, v170, v89, vcc
.Lat_A_full:
	v_max3_f32 v92, v82, v83, v84
	v_max3_f32 v93, v85, v86, v87
	v_max3_f32 v92, v92, v88, v89
	v_max_f32_e32 v92, v92, v93
	v_mov_b32_e32 v93, v92
	s_nop 1
	v_permlane16_swap_b32_e32 v92, v93
	v_max_f32_e32 v92, v92, v93
	v_mov_b32_e32 v93, v92
	s_nop 1
	v_permlane32_swap_b32_e32 v92, v93
	v_max_f32_e32 v92, v92, v93
	v_mul_f32_e32 v92, s25, v92
	v_max_f32_e32 v180, v181, v92
	v_sub_f32_e32 v94, v181, v180
	v_fma_f32 v82, v82, s25, -v180
	v_fma_f32 v83, v83, s25, -v180
	v_fma_f32 v84, v84, s25, -v180
	v_fma_f32 v85, v85, s25, -v180
	v_fma_f32 v86, v86, s25, -v180
	v_fma_f32 v87, v87, s25, -v180
	v_fma_f32 v88, v88, s25, -v180
	v_fma_f32 v89, v89, s25, -v180
	v_exp_f32_e32 v94, v94
	v_exp_f32_e32 v82, v82
	v_exp_f32_e32 v83, v83
	v_exp_f32_e32 v84, v84
	v_exp_f32_e32 v85, v85
	v_exp_f32_e32 v86, v86
	v_exp_f32_e32 v87, v87
	v_exp_f32_e32 v88, v88
	v_exp_f32_e32 v89, v89
	v_add_f32_e32 v92, v82, v83
	v_add_f32_e32 v93, v84, v85
	v_add_f32_e32 v97, v86, v87
	v_add_f32_e32 v92, v92, v93
	v_add_f32_e32 v96, v88, v89
	v_add_f32_e32 v97, v97, v96
	v_add_f32_e32 v92, v92, v97
	v_mov_b32_e32 v93, v92
	v_mov_b32_e32 v181, v180
	v_cvt_pk_bf16_f32 v82, v82, v83
	v_cvt_pk_bf16_f32 v83, v84, v85
	v_permlane16_swap_b32_e32 v92, v93
	v_add_f32_e32 v92, v92, v93
	v_mov_b32_e32 v93, v92
	v_cvt_pk_bf16_f32 v84, v86, v87
	v_cvt_pk_bf16_f32 v85, v88, v89
	v_permlane32_swap_b32_e32 v92, v93
	v_add_f32_e32 v92, v92, v93
	v_fma_f32 v179, v179, v94, v92
	v_pk_mul_f32 v[2:3], v[2:3], v[94:95] op_sel_hi:[1,0]
	v_pk_mul_f32 v[4:5], v[4:5], v[94:95] op_sel_hi:[1,0]
	v_pk_mul_f32 v[6:7], v[6:7], v[94:95] op_sel_hi:[1,0]
	v_pk_mul_f32 v[8:9], v[8:9], v[94:95] op_sel_hi:[1,0]
	v_pk_mul_f32 v[10:11], v[10:11], v[94:95] op_sel_hi:[1,0]
	v_pk_mul_f32 v[12:13], v[12:13], v[94:95] op_sel_hi:[1,0]
	v_pk_mul_f32 v[14:15], v[14:15], v[94:95] op_sel_hi:[1,0]
	v_pk_mul_f32 v[16:17], v[16:17], v[94:95] op_sel_hi:[1,0]
	v_pk_mul_f32 v[18:19], v[18:19], v[94:95] op_sel_hi:[1,0]
	v_pk_mul_f32 v[20:21], v[20:21], v[94:95] op_sel_hi:[1,0]
	v_pk_mul_f32 v[22:23], v[22:23], v[94:95] op_sel_hi:[1,0]
	v_pk_mul_f32 v[24:25], v[24:25], v[94:95] op_sel_hi:[1,0]
	v_pk_mul_f32 v[26:27], v[26:27], v[94:95] op_sel_hi:[1,0]
	v_pk_mul_f32 v[28:29], v[28:29], v[94:95] op_sel_hi:[1,0]
	v_pk_mul_f32 v[30:31], v[30:31], v[94:95] op_sel_hi:[1,0]
	v_pk_mul_f32 v[32:33], v[32:33], v[94:95] op_sel_hi:[1,0]
	ds_read_b64_tr_b16 v[86:87], v231
	ds_read_b64_tr_b16 v[88:89], v231 offset:4096
	ds_read_b64_tr_b16 v[244:245], v232
	ds_read_b64_tr_b16 v[246:247], v232 offset:4096
	s_waitcnt lgkmcnt(2)
	v_mfma_f32_16x16x32_bf16 v[2:5], v[86:89], v[82:85], v[2:5]
	ds_read_b64_tr_b16 v[86:87], v233
	ds_read_b64_tr_b16 v[88:89], v233 offset:4096
	s_waitcnt lgkmcnt(2)
	v_mfma_f32_16x16x32_bf16 v[6:9], v[244:247], v[82:85], v[6:9]
	ds_read_b64_tr_b16 v[244:245], v234
	ds_read_b64_tr_b16 v[246:247], v234 offset:4096
	s_waitcnt lgkmcnt(2)
	v_mfma_f32_16x16x32_bf16 v[10:13], v[86:89], v[82:85], v[10:13]
	ds_read_b64_tr_b16 v[86:87], v235
	ds_read_b64_tr_b16 v[88:89], v235 offset:4096
	s_waitcnt lgkmcnt(2)
	v_mfma_f32_16x16x32_bf16 v[14:17], v[244:247], v[82:85], v[14:17]
	ds_read_b64_tr_b16 v[244:245], v236
	ds_read_b64_tr_b16 v[246:247], v236 offset:4096
	s_waitcnt lgkmcnt(2)
	v_mfma_f32_16x16x32_bf16 v[18:21], v[86:89], v[82:85], v[18:21]
	ds_read_b64_tr_b16 v[86:87], v237
	ds_read_b64_tr_b16 v[88:89], v237 offset:4096
	s_waitcnt lgkmcnt(2)
	v_mfma_f32_16x16x32_bf16 v[22:25], v[244:247], v[82:85], v[22:25]
	ds_read_b64_tr_b16 v[244:245], v238
	ds_read_b64_tr_b16 v[246:247], v238 offset:4096
	s_waitcnt lgkmcnt(2)
	v_mfma_f32_16x16x32_bf16 v[30:33], v[86:89], v[82:85], v[30:33]
	s_waitcnt lgkmcnt(0)
	v_mfma_f32_16x16x32_bf16 v[26:29], v[244:247], v[82:85], v[26:29]
	s_add_u32 s11, s11, 1
	s_add_u32 s22, s22, 32
	v_add_u32_e32 v239, 0x80, v239
	s_cmp_lt_u32 s11, s10
	s_cbranch_scc0 .Lat_done

.Lat_B_nosel:
	s_waitcnt lgkmcnt(0)
	s_cmp_ge_u32 s23, 3
	s_cbranch_scc0 .Lat_B_tail
	v_mfma_f32_16x16x32_bf16 v[82:85], v[50:53], v[42:45], 0
	s_mov_b32 m0, s26
	v_mad_u32_u24 v240, v98, s35, v220
	global_load_lds_dwordx4 v240, s[4:5]
	s_add_u32 m0, s26, 1024
	v_mad_u32_u24 v240, v99, s35, v221
	global_load_lds_dwordx4 v240, s[4:5]
	v_mfma_f32_16x16x32_bf16 v[86:89], v[66:69], v[42:45], 0
	s_add_u32 m0, s26, 2048
	v_mad_u32_u24 v240, v100, s35, v222
	global_load_lds_dwordx4 v240, s[4:5]
	s_add_u32 m0, s26, 3072
	v_mad_u32_u24 v240, v101, s35, v223
	global_load_lds_dwordx4 v240, s[4:5]
	v_mfma_f32_16x16x32_bf16 v[82:85], v[54:57], v[34:37], v[82:85]
	s_add_u32 m0, s26, 4096
	v_mad_u32_u24 v240, v102, s35, v220
	global_load_lds_dwordx4 v240, s[4:5]
	s_add_u32 m0, s26, 5120
	v_mad_u32_u24 v240, v103, s35, v221
	global_load_lds_dwordx4 v240, s[4:5]
	v_mfma_f32_16x16x32_bf16 v[86:89], v[70:73], v[34:37], v[86:89]
	s_add_u32 m0, s26, 6144
	v_mad_u32_u24 v240, v104, s35, v222
	global_load_lds_dwordx4 v240, s[4:5]
	s_add_u32 m0, s26, 7168
	v_mad_u32_u24 v240, v105, s35, v223
	global_load_lds_dwordx4 v240, s[4:5]
	v_mfma_f32_16x16x32_bf16 v[82:85], v[58:61], v[38:41], v[82:85]
	v_mad_u32_u24 v240, v106, s35, v224
	global_load_dwordx4 v[188:191], v240, s[6:7]
	v_mad_u32_u24 v240, v107, s35, v224
	global_load_dwordx4 v[192:195], v240, s[6:7]
	v_mfma_f32_16x16x32_bf16 v[86:89], v[74:77], v[38:41], v[86:89]
	v_mad_u32_u24 v240, v108, s35, v224
	global_load_dwordx4 v[196:199], v240, s[6:7]
	v_mad_u32_u24 v240, v109, s35, v224
	global_load_dwordx4 v[200:203], v240, s[6:7]
	v_mfma_f32_16x16x32_bf16 v[82:85], v[62:65], v[46:49], v[82:85]
	v_mad_u32_u24 v240, v110, s35, v224
	global_load_dwordx4 v[204:207], v240, s[6:7]
	v_mad_u32_u24 v240, v111, s35, v224
	global_load_dwordx4 v[208:211], v240, s[6:7]
	v_mfma_f32_16x16x32_bf16 v[86:89], v[78:81], v[46:49], v[86:89]
	v_mad_u32_u24 v240, v112, s35, v224
	global_load_dwordx4 v[212:215], v240, s[6:7]
	v_mad_u32_u24 v240, v113, s35, v224
	global_load_dwordx4 v[216:219], v240, s[6:7]
	s_branch .Lat_B_sm
.Lat_B_tail:
	s_cmp_ge_u32 s23, 2
	s_cbranch_scc0 .Lat_B_nok
	s_mov_b32 m0, s26
	v_mad_u32_u24 v240, v98, s35, v220
	global_load_lds_dwordx4 v240, s[4:5]
	s_add_u32 m0, s26, 1024
	v_mad_u32_u24 v240, v99, s35, v221
	global_load_lds_dwordx4 v240, s[4:5]
	s_add_u32 m0, s26, 2048
	v_mad_u32_u24 v240, v100, s35, v222
	global_load_lds_dwordx4 v240, s[4:5]
	s_add_u32 m0, s26, 3072
	v_mad_u32_u24 v240, v101, s35, v223
	global_load_lds_dwordx4 v240, s[4:5]
	s_add_u32 m0, s26, 4096
	v_mad_u32_u24 v240, v102, s35, v220
	global_load_lds_dwordx4 v240, s[4:5]
	s_add_u32 m0, s26, 5120
	v_mad_u32_u24 v240, v103, s35, v221
	global_load_lds_dwordx4 v240, s[4:5]
	s_add_u32 m0, s26, 6144
	v_mad_u32_u24 v240, v104, s35, v222
	global_load_lds_dwordx4 v240, s[4:5]
	s_add_u32 m0, s26, 7168
	v_mad_u32_u24 v240, v105, s35, v223
	global_load_lds_dwordx4 v240, s[4:5]

.Lat_B_full:
	v_max3_f32 v92, v82, v83, v84
	v_max3_f32 v93, v85, v86, v87
	v_max3_f32 v92, v92, v88, v89
	v_max_f32_e32 v92, v92, v93
	v_mov_b32_e32 v93, v92
	s_nop 1
	v_permlane16_swap_b32_e32 v92, v93
	v_max_f32_e32 v92, v92, v93
	v_mov_b32_e32 v93, v92
	s_nop 1
	v_permlane32_swap_b32_e32 v92, v93
	v_max_f32_e32 v92, v92, v93
	v_mul_f32_e32 v92, s25, v92
	v_max_f32_e32 v180, v181, v92
	v_sub_f32_e32 v94, v181, v180
	v_fma_f32 v82, v82, s25, -v180
	v_fma_f32 v83, v83, s25, -v180
	v_fma_f32 v84, v84, s25, -v180
	v_fma_f32 v85, v85, s25, -v180
	v_fma_f32 v86, v86, s25, -v180
	v_fma_f32 v87, v87, s25, -v180
	v_fma_f32 v88, v88, s25, -v180
	v_fma_f32 v89, v89, s25, -v180
	v_exp_f32_e32 v94, v94
	v_exp_f32_e32 v82, v82
	v_exp_f32_e32 v83, v83
	v_exp_f32_e32 v84, v84
	v_exp_f32_e32 v85, v85
	v_exp_f32_e32 v86, v86
	v_exp_f32_e32 v87, v87
	v_exp_f32_e32 v88, v88
	v_exp_f32_e32 v89, v89
	v_add_f32_e32 v92, v82, v83
	v_add_f32_e32 v93, v84, v85
	v_add_f32_e32 v97, v86, v87
	v_add_f32_e32 v92, v92, v93
	v_add_f32_e32 v96, v88, v89
	v_add_f32_e32 v97, v97, v96
	v_add_f32_e32 v92, v92, v97
	v_mov_b32_e32 v93, v92
	v_mov_b32_e32 v181, v180
	v_cvt_pk_bf16_f32 v82, v82, v83
	v_cvt_pk_bf16_f32 v83, v84, v85
	v_permlane16_swap_b32_e32 v92, v93
	v_add_f32_e32 v92, v92, v93
	v_mov_b32_e32 v93, v92
	v_cvt_pk_bf16_f32 v84, v86, v87
	v_cvt_pk_bf16_f32 v85, v88, v89
	v_permlane32_swap_b32_e32 v92, v93
	v_add_f32_e32 v92, v92, v93
	v_fma_f32 v179, v179, v94, v92
	v_pk_mul_f32 v[2:3], v[2:3], v[94:95] op_sel_hi:[1,0]
	v_pk_mul_f32 v[4:5], v[4:5], v[94:95] op_sel_hi:[1,0]
	v_pk_mul_f32 v[6:7], v[6:7], v[94:95] op_sel_hi:[1,0]
	v_pk_mul_f32 v[8:9], v[8:9], v[94:95] op_sel_hi:[1,0]
	v_pk_mul_f32 v[10:11], v[10:11], v[94:95] op_sel_hi:[1,0]
	v_pk_mul_f32 v[12:13], v[12:13], v[94:95] op_sel_hi:[1,0]
	v_pk_mul_f32 v[14:15], v[14:15], v[94:95] op_sel_hi:[1,0]
	v_pk_mul_f32 v[16:17], v[16:17], v[94:95] op_sel_hi:[1,0]
	v_pk_mul_f32 v[18:19], v[18:19], v[94:95] op_sel_hi:[1,0]
	v_pk_mul_f32 v[20:21], v[20:21], v[94:95] op_sel_hi:[1,0]
	v_pk_mul_f32 v[22:23], v[22:23], v[94:95] op_sel_hi:[1,0]
	v_pk_mul_f32 v[24:25], v[24:25], v[94:95] op_sel_hi:[1,0]
	v_pk_mul_f32 v[26:27], v[26:27], v[94:95] op_sel_hi:[1,0]
	v_pk_mul_f32 v[28:29], v[28:29], v[94:95] op_sel_hi:[1,0]
	v_pk_mul_f32 v[30:31], v[30:31], v[94:95] op_sel_hi:[1,0]
	v_pk_mul_f32 v[32:33], v[32:33], v[94:95] op_sel_hi:[1,0]
	ds_read_b64_tr_b16 v[86:87], v231
	ds_read_b64_tr_b16 v[88:89], v231 offset:4096
	ds_read_b64_tr_b16 v[244:245], v232
	ds_read_b64_tr_b16 v[246:247], v232 offset:4096
	s_waitcnt lgkmcnt(2)
	v_mfma_f32_16x16x32_bf16 v[2:5], v[86:89], v[82:85], v[2:5]
	ds_read_b64_tr_b16 v[86:87], v233
	ds_read_b64_tr_b16 v[88:89], v233 offset:4096
	s_waitcnt lgkmcnt(2)
	v_mfma_f32_16x16x32_bf16 v[6:9], v[244:247], v[82:85], v[6:9]
	ds_read_b64_tr_b16 v[244:245], v234
	ds_read_b64_tr_b16 v[246:247], v234 offset:4096
	s_waitcnt lgkmcnt(2)
	v_mfma_f32_16x16x32_bf16 v[10:13], v[86:89], v[82:85], v[10:13]
	ds_read_b64_tr_b16 v[86:87], v235
	ds_read_b64_tr_b16 v[88:89], v235 offset:4096
	s_waitcnt lgkmcnt(2)
	v_mfma_f32_16x16x32_bf16 v[14:17], v[244:247], v[82:85], v[14:17]
	ds_read_b64_tr_b16 v[244:245], v236
	ds_read_b64_tr_b16 v[246:247], v236 offset:4096
	s_waitcnt lgkmcnt(2)
	v_mfma_f32_16x16x32_bf16 v[18:21], v[86:89], v[82:85], v[18:21]
	ds_read_b64_tr_b16 v[86:87], v237
	ds_read_b64_tr_b16 v[88:89], v237 offset:4096
	s_waitcnt lgkmcnt(2)
	v_mfma_f32_16x16x32_bf16 v[22:25], v[244:247], v[82:85], v[22:25]
	ds_read_b64_tr_b16 v[244:245], v238
	ds_read_b64_tr_b16 v[246:247], v238 offset:4096
	s_waitcnt lgkmcnt(2)
	v_mfma_f32_16x16x32_bf16 v[30:33], v[86:89], v[82:85], v[30:33]
	s_waitcnt lgkmcnt(0)
	v_mfma_f32_16x16x32_bf16 v[26:29], v[244:247], v[82:85], v[26:29]
	s_add_u32 s11, s11, 1
	s_add_u32 s22, s22, 32
	v_add_u32_e32 v239, 0x80, v239
	s_cmp_lt_u32 s11, s10
	s_cbranch_scc1 .Lat_A
